# retention main: the first wait covers only the ks piece and the q loads (counted vmcnt(8), loads only behind them); V piece 0 stays in flight through the QK^T block and is covered by the next wait+bar
# speedup vs baseline: 1.0037x; 1.0016x over previous
; #define GAS __attribute__((address_space(1)))
; #define RM_WAITBAR() asm volatile("s_waitcnt vmcnt(0) lgkmcnt(0)\n\ts_barrier" ::: "memory")
; #define RM_DMA_KS(buf) do { _Pragma("unroll") for (int i = 0; i < 8; ++i) { const int idx = tid + 512 * i, tok = idx >> 5, c = (idx & 31) ^ (tok & 31); \
;         glds16(PROJ + (size_t)T * 1024 + (hb0 + tok) * 256 + c * 8, (unsigned)__builtin_amdgcn_readfirstlane(ldsb + (buf) * 65536 + i * 8192)); } } while (0)
; #define RM_DMA_V(p, buf) do { _Pragma("unroll") for (int i = 0; i < 8; ++i) { const int idx = tid + 512 * i, tok = (idx >> 2) & 127; \
;         glds16(PROJ + (size_t)2 * T * 1024 + (hb0 + tok) * 512 + (p) * 256 + (idx >> 9) * 32 + (idx & 3) * 8, (unsigned)__builtin_amdgcn_readfirstlane(ldsb + (buf) * 65536 + i * 8192)); } } while (0)
; __device__ __forceinline__ void ret_main_phase(Frame& F, const bf16* PROJ, const bf16* ST, bf16* AO) { LTID();
;     ...
;         int tid = tid_; asm volatile("" : "+v"(tid));
;         const int lane = tid & 63, r32 = lane & 31, hh = lane >> 5, wid = __builtin_amdgcn_readfirstlane(tid >> 6), rg = wid & 3, e2 = wid >> 2;
;         const int voff = (4 * hh + ((lane & 15) >> 2)) * 64 + ((lane >> 4) & 1) * 32 + (lane & 3) * 8;
;         const int U = L + uu, bh = U >> 6, n = U & 63, b = bh >> 2, h = bh & 3;
;         const size_t tokbase = (size_t)b * SEQ + (size_t)n * 128, hb0 = (size_t)bh * SEQ + (size_t)n * 128;
;         const bf16* qrow = PROJ + (hb0 + rg * 32 + r32) * 256 + 8 * hh;
;         const bf16* stb = ST + ((size_t)bh * 64 + n) * 512 * 256;
;         const unsigned ldsb = (unsigned)(uintptr_t)lds + wid * 1024;
;     ...
;         RM_DMA_KS(0);
;         bf16x8 pa[4][2];
;         {
;             bf16x8 qf[16];
; #pragma unroll
;             for (int s = 0; s < 16; ++s) qf[s] = *(const GAS bf16x8*)(qrow + 16 * s);
;             RM_WAITBAR();
;             asm volatile("" :: "v"(qf[0]), "v"(qf[1]), "v"(qf[2]), "v"(qf[3]), "v"(qf[4]), "v"(qf[5]), "v"(qf[6]), "v"(qf[7]), "v"(qf[8]), "v"(qf[9]), "v"(qf[10]), "v"(qf[11]), "v"(qf[12]), "v"(qf[13]), "v"(qf[14]), "v"(qf[15]));
;             RM_DMA_V(0, 1);
.LBB0_365:
	v_mov_b32_e32 v210, v202
	s_nop 0
	v_readfirstlane_b32 s61, v210
	s_ashr_i32 s0, s61, 6
	s_and_b32 s66, s0, 3
	s_lshl_b32 s64, s66, 5
	v_and_b32_e32 v213, 31, v210
	s_add_u32 s34, s24, s30
	s_waitcnt vmcnt(0)
	v_ashrrev_i32_e32 v4, 5, v210
	v_or_b32_e32 v0, s64, v213
	s_addc_u32 s35, s25, s31
	v_ashrrev_i32_e32 v5, 31, v4
	v_lshl_add_u64 v[2:3], s[34:35], 0, v[0:1]
	v_xor_b32_e32 v0, v4, v210
	v_lshl_add_u64 v[4:5], s[34:35], 0, v[4:5]
	v_lshlrev_b64 v[4:5], 9, v[4:5]
	v_lshlrev_b32_e32 v0, 4, v0
	v_lshl_add_u64 v[4:5], s[14:15], 0, v[4:5]
	v_and_b32_e32 v0, 0x1f0, v0
	s_lshl_b32 s0, s0, 10
	v_lshl_add_u64 v[4:5], v[4:5], 0, v[0:1]
	v_add_u32_e32 v209, 0x200, v210
	s_add_i32 s65, s0, 0
	s_mov_b32 m0, s65
	s_nop 0
	global_load_lds_dwordx4 v[4:5], off
	v_ashrrev_i32_e32 v4, 5, v209
	v_ashrrev_i32_e32 v5, 31, v4
	v_xor_b32_e32 v0, v4, v210
	v_lshl_add_u64 v[4:5], s[34:35], 0, v[4:5]
	v_lshlrev_b64 v[4:5], 9, v[4:5]
	v_lshlrev_b32_e32 v0, 4, v0
	v_lshl_add_u64 v[4:5], s[14:15], 0, v[4:5]
	v_and_b32_e32 v0, 0x1f0, v0
	v_lshl_add_u64 v[4:5], v[4:5], 0, v[0:1]
	v_add_u32_e32 v208, 0x400, v210
	s_add_i32 s68, s65, 0x2000
	s_mov_b32 m0, s68
	s_nop 0
	global_load_lds_dwordx4 v[4:5], off
	v_ashrrev_i32_e32 v4, 5, v208
	v_ashrrev_i32_e32 v5, 31, v4
	v_xor_b32_e32 v0, v4, v210
	v_lshl_add_u64 v[4:5], s[34:35], 0, v[4:5]
	v_lshlrev_b64 v[4:5], 9, v[4:5]
	v_lshlrev_b32_e32 v0, 4, v0
	v_lshl_add_u64 v[4:5], s[14:15], 0, v[4:5]
	v_and_b32_e32 v0, 0x1f0, v0
	v_lshl_add_u64 v[4:5], v[4:5], 0, v[0:1]
	v_add_u32_e32 v207, 0x600, v210
	s_add_i32 s69, s65, 0x4000
	s_mov_b32 m0, s69
	s_nop 0
	global_load_lds_dwordx4 v[4:5], off
	v_ashrrev_i32_e32 v4, 5, v207
	v_ashrrev_i32_e32 v5, 31, v4
	v_xor_b32_e32 v0, v4, v210
	v_lshl_add_u64 v[4:5], s[34:35], 0, v[4:5]
	v_lshlrev_b64 v[4:5], 9, v[4:5]
	v_lshlrev_b32_e32 v0, 4, v0
	v_lshl_add_u64 v[4:5], s[14:15], 0, v[4:5]
	v_and_b32_e32 v0, 0x1f0, v0
	v_lshl_add_u64 v[4:5], v[4:5], 0, v[0:1]
	v_add_u32_e32 v206, 0x800, v210
	s_add_i32 s70, s65, 0x6000
	s_mov_b32 m0, s70
	s_nop 0
	global_load_lds_dwordx4 v[4:5], off
	v_ashrrev_i32_e32 v4, 5, v206
	v_ashrrev_i32_e32 v5, 31, v4
	v_xor_b32_e32 v0, v4, v210
	v_lshl_add_u64 v[4:5], s[34:35], 0, v[4:5]
	v_lshlrev_b64 v[4:5], 9, v[4:5]
	v_lshlrev_b32_e32 v0, 4, v0
	v_lshl_add_u64 v[4:5], s[14:15], 0, v[4:5]
	v_and_b32_e32 v0, 0x1f0, v0
	v_lshl_add_u64 v[4:5], v[4:5], 0, v[0:1]
	v_add_u32_e32 v205, 0xa00, v210
	s_add_i32 s46, s65, 0x8000
	s_mov_b32 m0, s46
	s_nop 0
	global_load_lds_dwordx4 v[4:5], off
	v_ashrrev_i32_e32 v4, 5, v205
	v_ashrrev_i32_e32 v5, 31, v4
	v_xor_b32_e32 v0, v4, v210
	v_lshl_add_u64 v[4:5], s[34:35], 0, v[4:5]
	v_lshlrev_b64 v[4:5], 9, v[4:5]
	v_lshlrev_b32_e32 v0, 4, v0
	v_lshl_add_u64 v[4:5], s[14:15], 0, v[4:5]
	v_and_b32_e32 v0, 0x1f0, v0
	v_lshl_add_u64 v[4:5], v[4:5], 0, v[0:1]
	v_add_u32_e32 v204, 0xc00, v210
	s_add_i32 s42, s65, 0xa000
	s_mov_b32 m0, s42
	s_nop 0
	global_load_lds_dwordx4 v[4:5], off
	v_ashrrev_i32_e32 v4, 5, v204
	v_ashrrev_i32_e32 v5, 31, v4
	v_xor_b32_e32 v0, v4, v210
	v_lshl_add_u64 v[4:5], s[34:35], 0, v[4:5]
	v_lshlrev_b64 v[4:5], 9, v[4:5]
	v_lshlrev_b32_e32 v0, 4, v0
	v_lshl_add_u64 v[4:5], s[14:15], 0, v[4:5]
	v_and_b32_e32 v0, 0x1f0, v0
	v_lshl_add_u64 v[4:5], v[4:5], 0, v[0:1]
	v_add_u32_e32 v203, 0xe00, v210
	s_add_i32 s47, s65, 0xc000
	s_mov_b32 m0, s47
	s_nop 0
	global_load_lds_dwordx4 v[4:5], off
	v_ashrrev_i32_e32 v4, 5, v203
	v_ashrrev_i32_e32 v5, 31, v4
	v_xor_b32_e32 v0, v4, v210
	v_lshl_add_u64 v[4:5], s[34:35], 0, v[4:5]
	v_lshlrev_b64 v[4:5], 9, v[4:5]
	v_lshlrev_b32_e32 v0, 4, v0
	v_bfe_u32 v180, v210, 5, 1
	v_lshlrev_b64 v[2:3], 9, v[2:3]
	v_lshl_add_u64 v[4:5], s[14:15], 0, v[4:5]
	v_and_b32_e32 v0, 0x1f0, v0
	v_lshl_add_u64 v[4:5], v[4:5], 0, v[0:1]
	v_lshl_add_u64 v[2:3], s[12:13], 0, v[2:3]
	v_lshlrev_b32_e32 v0, 4, v180
	s_add_i32 s50, s65, 0xe000
	s_mov_b32 m0, s50
	s_nop 0
	global_load_lds_dwordx4 v[4:5], off
	v_lshl_add_u64 v[162:163], v[2:3], 0, v[0:1]
	global_load_dwordx4 v[34:37], v[162:163], off
	global_load_dwordx4 v[122:125], v[162:163], off offset:32
	global_load_dwordx4 v[118:121], v[162:163], off offset:64
	global_load_dwordx4 v[114:117], v[162:163], off offset:96
	global_load_dwordx4 v[110:113], v[162:163], off offset:128
	global_load_dwordx4 v[106:109], v[162:163], off offset:160
	global_load_dwordx4 v[102:105], v[162:163], off offset:192
	global_load_dwordx4 v[98:101], v[162:163], off offset:224
	global_load_dwordx4 v[94:97], v[162:163], off offset:256
	global_load_dwordx4 v[90:93], v[162:163], off offset:288
	global_load_dwordx4 v[82:85], v[162:163], off offset:320
	global_load_dwordx4 v[86:89], v[162:163], off offset:352
	global_load_dwordx4 v[62:65], v[162:163], off offset:384
	global_load_dwordx4 v[58:61], v[162:163], off offset:416
	global_load_dwordx4 v[54:57], v[162:163], off offset:448
	global_load_dwordx4 v[50:53], v[162:163], off offset:480
	v_bfe_u32 v0, v210, 2, 7
	v_lshlrev_b32_e32 v211, 3, v210
	v_lshl_add_u64 v[2:3], s[34:35], 0, v[0:1]
	v_and_b32_e32 v127, 24, v211
	v_lshlrev_b64 v[142:143], 10, v[2:3]
	v_ashrrev_i32_e32 v170, 4, v210
	v_lshl_add_u64 v[2:3], s[18:19], 0, v[142:143]
	v_lshlrev_b32_e32 v0, 1, v127
	v_and_b32_e32 v144, 0xffffffe0, v170
	v_ashrrev_i32_e32 v168, 4, v209
	v_lshl_add_u64 v[2:3], v[2:3], 0, v[0:1]
	v_ashrrev_i32_e32 v145, 31, v144
	v_and_b32_e32 v146, 0xffffffe0, v168
	v_ashrrev_i32_e32 v166, 4, v208
	s_add_i32 s0, s65, 0x10000
	v_lshl_add_u64 v[4:5], v[144:145], 1, v[2:3]
	v_ashrrev_i32_e32 v147, 31, v146
	v_and_b32_e32 v148, 0xffffffe0, v166
	v_ashrrev_i32_e32 v164, 4, v207
	s_mov_b32 m0, s0
	s_nop 0
	global_load_lds_dwordx4 v[4:5], off
; #define LAS __attribute__((address_space(3)))
; __device__ __forceinline__ int crow(int r, int hi) { return (r & 3) + 8 * (r >> 2) + 4 * hi; }
; #define RM_WAITBAR() asm volatile("s_waitcnt vmcnt(0) lgkmcnt(0)\n\ts_barrier" ::: "memory")
; #define RM_DMA_V(p, buf) do { _Pragma("unroll") for (int i = 0; i < 8; ++i) { const int idx = tid + 512 * i, tok = (idx >> 2) & 127; \
;         glds16(PROJ + (size_t)2 * T * 1024 + (hb0 + tok) * 512 + (p) * 256 + (idx >> 9) * 32 + (idx & 3) * 8, (unsigned)__builtin_amdgcn_readfirstlane(ldsb + (buf) * 65536 + i * 8192)); } } while (0)
; __device__ __forceinline__ void ret_main_phase(Frame& F, const bf16* PROJ, const bf16* ST, bf16* AO) { LTID();
;     ...
;             RM_WAITBAR();
;             asm volatile("" :: "v"(qf[0]), "v"(qf[1]), "v"(qf[2]), "v"(qf[3]), "v"(qf[4]), "v"(qf[5]), "v"(qf[6]), "v"(qf[7]), "v"(qf[8]), "v"(qf[9]), "v"(qf[10]), "v"(qf[11]), "v"(qf[12]), "v"(qf[13]), "v"(qf[14]), "v"(qf[15]));
;             RM_DMA_V(0, 1);
; #pragma unroll
;             for (int jb = 0; jb < 4; ++jb) {
;                 f32x16 S = (f32x16){0.f, 0.f, 0.f, 0.f, 0.f, 0.f, 0.f, 0.f, 0.f, 0.f, 0.f, 0.f, 0.f, 0.f, 0.f, 0.f};
;                 if (jb <= rg) {
; #pragma unroll
;                     for (int s = 0; s < 16; ++s) { const bf16x8 a = *(const LAS bf16x8*)(lds + (32 * jb + r32) * 512 + (((2 * s + hh) ^ r32) * 16)); S = __builtin_amdgcn_mfma_f32_32x32x16_bf16(a, qf[s], S, 0, 0, 0); }
;                     if (jb == rg) {
; #pragma unroll
;                         for (int i = 0; i < 16; ++i) if (crow(i, hh) > r32) S[i] = 0.f; }
	v_lshl_add_u64 v[4:5], v[146:147], 1, v[2:3]
	s_add_i32 s43, s65, 0x12000
	s_mov_b32 m0, s43
	s_nop 0
	global_load_lds_dwordx4 v[4:5], off
	v_ashrrev_i32_e32 v149, 31, v148
	v_and_b32_e32 v150, 0xffffffe0, v164
	v_ashrrev_i32_e32 v160, 4, v206
	v_lshl_add_u64 v[4:5], v[148:149], 1, v[2:3]
	s_add_i32 s44, s65, 0x14000
	s_mov_b32 m0, s44
	s_nop 0
	global_load_lds_dwordx4 v[4:5], off
	v_ashrrev_i32_e32 v151, 31, v150
	v_and_b32_e32 v152, 0xffffffe0, v160
	v_ashrrev_i32_e32 v158, 4, v205
	v_lshl_add_u64 v[4:5], v[150:151], 1, v[2:3]
	s_add_i32 s45, s65, 0x16000
	s_mov_b32 m0, s45
	s_nop 0
	global_load_lds_dwordx4 v[4:5], off
	v_ashrrev_i32_e32 v153, 31, v152
	v_and_b32_e32 v154, 0xffffffe0, v158
	v_ashrrev_i32_e32 v128, 4, v204
	v_ashrrev_i32_e32 v126, 4, v203
	v_lshl_add_u64 v[4:5], v[152:153], 1, v[2:3]
	s_add_i32 s51, s65, 0x18000
	s_mov_b32 m0, s51
	s_nop 0
	global_load_lds_dwordx4 v[4:5], off
	v_ashrrev_i32_e32 v155, 31, v154
	v_and_b32_e32 v156, 0xffffffe0, v128
	v_and_b32_e32 v172, 0xffffffe0, v126
	v_lshl_add_u64 v[4:5], v[154:155], 1, v[2:3]
	s_add_i32 s56, s65, 0x1a000
	s_mov_b32 m0, s56
	s_nop 0
	global_load_lds_dwordx4 v[4:5], off
	v_ashrrev_i32_e32 v157, 31, v156
	v_ashrrev_i32_e32 v173, 31, v172
	v_lshrrev_b32_e32 v6, 5, v210
	v_lshl_add_u64 v[4:5], v[156:157], 1, v[2:3]
	s_add_i32 s62, s65, 0x1c000
	s_mov_b32 m0, s62
	s_nop 0
	global_load_lds_dwordx4 v[4:5], off
	v_lshl_add_u64 v[2:3], v[172:173], 1, v[2:3]
	s_add_i32 s63, s65, 0x1e000
	s_mov_b32 m0, s63
	s_nop 0
	global_load_lds_dwordx4 v[2:3], off
	s_waitcnt vmcnt(8) lgkmcnt(0)
	s_barrier
	v_bitop3_b32 v2, v6, v213, 1 bitop3:0x6c
	v_lshl_add_u32 v22, v213, 9, 0
	v_lshlrev_b32_e32 v2, 4, v2
	v_add_u32_e32 v38, v22, v2
	ds_read_b128 v[2:5], v38
	v_bitop3_b32 v18, v180, v213, 2 bitop3:0x36
	v_lshlrev_b32_e32 v18, 4, v18
	v_add_u32_e32 v39, v22, v18
	ds_read_b128 v[18:21], v39
	s_waitcnt lgkmcnt(1)
	v_mfma_f32_32x32x16_bf16 v[2:17], v[2:5], v[34:37], 0
	s_cmp_lg_u32 s66, 0
	s_cselect_b64 s[8:9], -1, 0
	v_lshlrev_b32_e32 v214, 2, v180
	s_and_b64 vcc, exec, s[8:9]
	s_waitcnt lgkmcnt(0)
	v_mfma_f32_32x32x16_bf16 v[2:17], v[18:21], v[122:125], v[2:17]
	v_bitop3_b32 v18, v180, v213, 4 bitop3:0x36
	v_lshlrev_b32_e32 v18, 4, v18
	v_add_u32_e32 v129, v22, v18
	ds_read_b128 v[18:21], v129
	s_waitcnt lgkmcnt(0)
	v_mfma_f32_32x32x16_bf16 v[2:17], v[18:21], v[118:121], v[2:17]
	v_bitop3_b32 v18, v180, v213, 6 bitop3:0x36
	v_lshlrev_b32_e32 v18, 4, v18
	v_add_u32_e32 v130, v22, v18
	ds_read_b128 v[18:21], v130
	s_waitcnt lgkmcnt(0)
	v_mfma_f32_32x32x16_bf16 v[2:17], v[18:21], v[114:117], v[2:17]
	v_bitop3_b32 v18, v180, v213, 8 bitop3:0x36
	v_lshlrev_b32_e32 v18, 4, v18
	v_add_u32_e32 v131, v22, v18
	ds_read_b128 v[18:21], v131
	s_waitcnt lgkmcnt(0)
	v_mfma_f32_32x32x16_bf16 v[2:17], v[18:21], v[110:113], v[2:17]
	v_bitop3_b32 v18, v180, v213, 10 bitop3:0x36
	v_lshlrev_b32_e32 v18, 4, v18
	v_add_u32_e32 v132, v22, v18
	ds_read_b128 v[18:21], v132
	s_waitcnt lgkmcnt(0)
	v_mfma_f32_32x32x16_bf16 v[2:17], v[18:21], v[106:109], v[2:17]
	v_bitop3_b32 v18, v180, v213, 12 bitop3:0x36
	v_lshlrev_b32_e32 v18, 4, v18
	v_add_u32_e32 v133, v22, v18
	ds_read_b128 v[18:21], v133
	s_waitcnt lgkmcnt(0)
	v_mfma_f32_32x32x16_bf16 v[2:17], v[18:21], v[102:105], v[2:17]
	v_bitop3_b32 v18, v180, v213, 14 bitop3:0x36
	v_lshlrev_b32_e32 v18, 4, v18
	v_add_u32_e32 v134, v22, v18
	ds_read_b128 v[18:21], v134
	s_waitcnt lgkmcnt(0)
	v_mfma_f32_32x32x16_bf16 v[2:17], v[18:21], v[98:101], v[2:17]
	v_bitop3_b32 v18, v180, v213, 16 bitop3:0x36
	v_lshlrev_b32_e32 v18, 4, v18
	v_add_u32_e32 v135, v22, v18
	ds_read_b128 v[18:21], v135
	s_waitcnt lgkmcnt(0)
	v_mfma_f32_32x32x16_bf16 v[2:17], v[18:21], v[94:97], v[2:17]
	v_bitop3_b32 v18, v180, v213, 18 bitop3:0x36
	v_lshlrev_b32_e32 v18, 4, v18
	v_add_u32_e32 v136, v22, v18
	ds_read_b128 v[18:21], v136
	s_waitcnt lgkmcnt(0)
	v_mfma_f32_32x32x16_bf16 v[2:17], v[18:21], v[90:93], v[2:17]
	v_bitop3_b32 v18, v180, v213, 20 bitop3:0x36
	v_lshlrev_b32_e32 v18, 4, v18
	v_add_u32_e32 v137, v22, v18
	ds_read_b128 v[18:21], v137
	s_waitcnt lgkmcnt(0)
	v_mfma_f32_32x32x16_bf16 v[2:17], v[18:21], v[82:85], v[2:17]
	v_bitop3_b32 v18, v180, v213, 22 bitop3:0x36
	v_lshlrev_b32_e32 v18, 4, v18
	v_add_u32_e32 v138, v22, v18
	ds_read_b128 v[18:21], v138
	s_waitcnt lgkmcnt(0)
	v_mfma_f32_32x32x16_bf16 v[2:17], v[18:21], v[86:89], v[2:17]
	v_bitop3_b32 v18, v180, v213, 24 bitop3:0x36
	v_lshlrev_b32_e32 v18, 4, v18
	v_add_u32_e32 v139, v22, v18
	ds_read_b128 v[18:21], v139
	s_waitcnt lgkmcnt(0)
	v_mfma_f32_32x32x16_bf16 v[2:17], v[18:21], v[62:65], v[2:17]
	v_bitop3_b32 v18, v180, v213, 26 bitop3:0x36
	v_lshlrev_b32_e32 v18, 4, v18
	v_add_u32_e32 v140, v22, v18
	ds_read_b128 v[18:21], v140
	s_waitcnt lgkmcnt(0)
	v_mfma_f32_32x32x16_bf16 v[2:17], v[18:21], v[58:61], v[2:17]
	v_bitop3_b32 v18, v180, v213, 28 bitop3:0x36
	v_lshlrev_b32_e32 v18, 4, v18
	v_add_u32_e32 v141, v22, v18
	ds_read_b128 v[18:21], v141
	s_waitcnt lgkmcnt(0)
	v_mfma_f32_32x32x16_bf16 v[2:17], v[18:21], v[54:57], v[2:17]
	v_bitop3_b32 v18, v180, v213, 30 bitop3:0x36
	v_lshlrev_b32_e32 v18, 4, v18
	v_add_u32_e32 v159, v22, v18
	ds_read_b128 v[18:21], v159
	s_waitcnt lgkmcnt(0)
	v_mfma_f32_32x32x16_bf16 v[2:17], v[18:21], v[50:53], v[2:17]
	s_cbranch_vccnz .LBB0_367
	v_cmp_lt_u32_e32 vcc, v214, v213
	v_or_b32_e32 v18, 2, v214
	s_nop 8
	v_cndmask_b32_e32 v3, 0, v3, vcc
	v_cmp_le_u32_e32 vcc, v214, v213
	s_nop 1
	v_cndmask_b32_e32 v2, 0, v2, vcc
	v_cmp_le_u32_e32 vcc, v18, v213
	v_or_b32_e32 v18, 3, v214
	s_nop 0
	v_cndmask_b32_e32 v4, 0, v4, vcc
	v_cmp_le_u32_e32 vcc, v18, v213
	v_or_b32_e32 v18, 8, v214
	s_nop 0
	v_cndmask_b32_e32 v5, 0, v5, vcc
	v_cmp_le_u32_e32 vcc, v18, v213
	v_or_b32_e32 v18, 9, v214
	s_nop 0
	v_cndmask_b32_e32 v6, 0, v6, vcc
	v_cmp_le_u32_e32 vcc, v18, v213
	v_or_b32_e32 v18, 10, v214
	s_nop 0
	v_cndmask_b32_e32 v7, 0, v7, vcc
	v_cmp_le_u32_e32 vcc, v18, v213
	v_or_b32_e32 v18, 11, v214
	s_nop 0
	v_cndmask_b32_e32 v8, 0, v8, vcc
	v_cmp_le_u32_e32 vcc, v18, v213
	v_or_b32_e32 v18, 16, v214
	s_nop 0
	v_cndmask_b32_e32 v9, 0, v9, vcc
	v_cmp_le_u32_e32 vcc, v18, v213
	v_or_b32_e32 v18, 17, v214
	s_nop 0
	v_cndmask_b32_e32 v10, 0, v10, vcc
	v_cmp_le_u32_e32 vcc, v18, v213
	v_or_b32_e32 v18, 18, v214
	s_nop 0
	v_cndmask_b32_e32 v11, 0, v11, vcc
	v_cmp_le_u32_e32 vcc, v18, v213
	v_or_b32_e32 v18, 19, v214
	s_nop 0
	v_cndmask_b32_e32 v12, 0, v12, vcc
	v_cmp_le_u32_e32 vcc, v18, v213
	v_or_b32_e32 v18, 24, v214
	s_nop 0
	v_cndmask_b32_e32 v13, 0, v13, vcc
	v_cmp_le_u32_e32 vcc, v18, v213
	v_or_b32_e32 v18, 25, v214
	s_nop 0
	v_cndmask_b32_e32 v14, 0, v14, vcc
	v_cmp_le_u32_e32 vcc, v18, v213
	v_or_b32_e32 v18, 26, v214
	s_nop 0
	v_cndmask_b32_e32 v15, 0, v15, vcc
	v_cmp_le_u32_e32 vcc, v18, v213
	v_or_b32_e32 v18, 27, v214
	s_nop 0
	v_cndmask_b32_e32 v16, 0, v16, vcc
	v_cmp_le_u32_e32 vcc, v18, v213
	s_nop 1
	v_cndmask_b32_e32 v17, 0, v17, vcc
